# DSA key-list building: dense lanes (more than 8 selected keys in 64) expanded by the whole wave (EXEC = lane mask, position = prefix + mbcnt), other lanes by a straight-line 8-step 64-bit lowest-bit l
# baseline (speedup 1.0000x reference)
.LBB0_700:
	v_add_u32_e32 v0, s46, v55
	s_waitcnt lgkmcnt(0)
	ds_read_b64 v[4:5], v0
	s_waitcnt lgkmcnt(0)
	v_bcnt_u32_b32 v0, v4, 0
	v_bcnt_u32_b32 v0, v5, v0
	v_mov_b64_e32 v[204:205], v[4:5]
	v_mov_b32_e32 v18, v0
	s_nop 1
	v_add_u32_dpp v18, v18, v18 row_shr:1 row_mask:0xf bank_mask:0xf
	s_nop 1
	v_add_u32_dpp v18, v18, v18 row_shr:2 row_mask:0xf bank_mask:0xf
	s_nop 1
	v_add_u32_dpp v18, v18, v18 row_shr:4 row_mask:0xf bank_mask:0xf
	s_nop 1
	v_add_u32_dpp v18, v18, v18 row_shr:8 row_mask:0xf bank_mask:0xf
	s_nop 1
	v_add_u32_dpp v18, v18, v18 row_bcast:15 row_mask:0xa bank_mask:0xf
	s_nop 1
	v_add_u32_dpp v18, v18, v18 row_bcast:31 row_mask:0xc bank_mask:0xf
	v_sub_u32_e32 v206, v18, v0
	v_cmp_lt_u32_e32 vcc, 8, v0
	s_mov_b64 s[100:101], vcc
	v_cndmask_b32_e32 v0, v0, v1, vcc
	v_sub_u32_e32 v13, s87, v206
	v_min_i32_e32 v0, v0, v13
	v_readlane_b32 s28, v18, 63
	v_lshl_add_u32 v12, v206, 1, s40
	v_cmpx_lt_i32_e32 vcc, 0, v0
	v_ffbl_b32_e32 v13, v4
	v_ffbl_b32_e32 v14, v5
	v_or_b32_e32 v14, 32, v14
	v_min_u32_e32 v13, v13, v14
	v_or_b32_e32 v13, v13, v8
	ds_write_b16 v12, v13
	v_add_co_u32_e32 v15, vcc, -1, v4
	v_addc_co_u32_e32 v16, vcc, -1, v5, vcc
	v_and_b32_e32 v4, v4, v15
	v_and_b32_e32 v5, v5, v16
	v_add_u32_e32 v12, 2, v12
	v_cmpx_lt_i32_e32 vcc, 1, v0
	v_ffbl_b32_e32 v13, v4
	v_ffbl_b32_e32 v14, v5
	v_or_b32_e32 v14, 32, v14
	v_min_u32_e32 v13, v13, v14
	v_or_b32_e32 v13, v13, v8
	ds_write_b16 v12, v13
	v_add_co_u32_e32 v15, vcc, -1, v4
	v_addc_co_u32_e32 v16, vcc, -1, v5, vcc
	v_and_b32_e32 v4, v4, v15
	v_and_b32_e32 v5, v5, v16
	v_add_u32_e32 v12, 2, v12
	v_cmpx_lt_i32_e32 vcc, 2, v0
	v_ffbl_b32_e32 v13, v4
	v_ffbl_b32_e32 v14, v5
	v_or_b32_e32 v14, 32, v14
	v_min_u32_e32 v13, v13, v14
	v_or_b32_e32 v13, v13, v8
	ds_write_b16 v12, v13
	v_add_co_u32_e32 v15, vcc, -1, v4
	v_addc_co_u32_e32 v16, vcc, -1, v5, vcc
	v_and_b32_e32 v4, v4, v15
	v_and_b32_e32 v5, v5, v16
	v_add_u32_e32 v12, 2, v12
	v_cmpx_lt_i32_e32 vcc, 3, v0
	v_ffbl_b32_e32 v13, v4
	v_ffbl_b32_e32 v14, v5
	v_or_b32_e32 v14, 32, v14
	v_min_u32_e32 v13, v13, v14
	v_or_b32_e32 v13, v13, v8
	ds_write_b16 v12, v13
	v_add_co_u32_e32 v15, vcc, -1, v4
	v_addc_co_u32_e32 v16, vcc, -1, v5, vcc
	v_and_b32_e32 v4, v4, v15
	v_and_b32_e32 v5, v5, v16
	v_add_u32_e32 v12, 2, v12
	v_cmpx_lt_i32_e32 vcc, 4, v0
	v_ffbl_b32_e32 v13, v4
	v_ffbl_b32_e32 v14, v5
	v_or_b32_e32 v14, 32, v14
	v_min_u32_e32 v13, v13, v14
	v_or_b32_e32 v13, v13, v8
	ds_write_b16 v12, v13
	v_add_co_u32_e32 v15, vcc, -1, v4
	v_addc_co_u32_e32 v16, vcc, -1, v5, vcc
	v_and_b32_e32 v4, v4, v15
	v_and_b32_e32 v5, v5, v16
	v_add_u32_e32 v12, 2, v12
	v_cmpx_lt_i32_e32 vcc, 5, v0
	v_ffbl_b32_e32 v13, v4
	v_ffbl_b32_e32 v14, v5
	v_or_b32_e32 v14, 32, v14
	v_min_u32_e32 v13, v13, v14
	v_or_b32_e32 v13, v13, v8
	ds_write_b16 v12, v13
	v_add_co_u32_e32 v15, vcc, -1, v4
	v_addc_co_u32_e32 v16, vcc, -1, v5, vcc
	v_and_b32_e32 v4, v4, v15
	v_and_b32_e32 v5, v5, v16
	v_add_u32_e32 v12, 2, v12
	v_cmpx_lt_i32_e32 vcc, 6, v0
	v_ffbl_b32_e32 v13, v4
	v_ffbl_b32_e32 v14, v5
	v_or_b32_e32 v14, 32, v14
	v_min_u32_e32 v13, v13, v14
	v_or_b32_e32 v13, v13, v8
	ds_write_b16 v12, v13
	v_add_co_u32_e32 v15, vcc, -1, v4
	v_addc_co_u32_e32 v16, vcc, -1, v5, vcc
	v_and_b32_e32 v4, v4, v15
	v_and_b32_e32 v5, v5, v16
	v_add_u32_e32 v12, 2, v12
	v_cmpx_lt_i32_e32 vcc, 7, v0
	v_ffbl_b32_e32 v13, v4
	v_ffbl_b32_e32 v14, v5
	v_or_b32_e32 v14, 32, v14
	v_min_u32_e32 v13, v13, v14
	v_or_b32_e32 v13, v13, v8
	ds_write_b16 v12, v13
	v_add_co_u32_e32 v15, vcc, -1, v4
	v_addc_co_u32_e32 v16, vcc, -1, v5, vcc
	v_and_b32_e32 v4, v4, v15
	v_and_b32_e32 v5, v5, v16
	v_add_u32_e32 v12, 2, v12
	s_mov_b64 exec, -1
	s_mov_b64 s[12:13], s[100:101]
	s_cmp_eq_u64 s[12:13], 0
	s_cbranch_scc1 .Llist_dx_a
.Llist_d_a:
	s_ff1_i32_b64 s100, s[12:13]
	s_bitset0_b64 s[12:13], s100
	v_readlane_b32 s26, v204, s100
	v_readlane_b32 s27, v205, s100
	v_readlane_b32 s101, v206, s100
	s_lshl_b32 s0, s100, 6
	s_nop 0
	v_mbcnt_lo_u32_b32 v13, s26, 0
	v_mbcnt_hi_u32_b32 v13, s27, v13
	v_add_u32_e32 v13, s101, v13
	v_cmp_gt_i32_e32 vcc, s87, v13
	s_and_b64 s[26:27], s[26:27], vcc
	v_add_u32_e32 v14, s0, v42
	v_lshl_add_u32 v13, v13, 1, s40
	s_mov_b64 exec, s[26:27]
	ds_write_b16 v13, v14
	s_mov_b64 exec, -1
	s_cmp_lg_u64 s[12:13], 0
	s_cbranch_scc1 .Llist_d_a
.Llist_dx_a:
	s_mov_b64 s[0:1], -1
.LBB0_711:
	s_or_b64 exec, exec, s[0:1]
	s_min_i32 s12, s28, 0x100
	v_add_u32_e32 v0, s12, v42
	v_cmp_gt_i32_e32 vcc, s87, v0
	s_and_saveexec_b64 s[0:1], vcc
	s_cbranch_execz .LBB0_583
	v_lshlrev_b32_e32 v0, 1, v0
	v_add_u32_e32 v4, s12, v11
	s_mov_b64 s[12:13], 0

.Llist_dx_b:
	s_mov_b64 s[0:1], -1
.LBB0_1089:
	s_or_b64 exec, exec, s[0:1]
	s_min_i32 s12, s28, 0x100
	v_add_u32_e32 v0, s12, v42
	v_cmp_gt_i32_e32 vcc, s87, v0
	s_and_saveexec_b64 s[0:1], vcc
	s_cbranch_execz .LBB0_961
	v_lshlrev_b32_e32 v0, 1, v0
	v_add_u32_e32 v4, s12, v11
	s_mov_b64 s[12:13], 0
